# layer-1 (fp8) out-proj epilogue: bf16 residual loads and row stores lane-transposed through ds_bpermute
# baseline (speedup 1.0000x reference)
; #define PG8_RSRC(base) __builtin_amdgcn_make_buffer_rsrc((void*)(base), (short)0, -1, 0x00020000)
; #define PG8_ST16(rs, b0, p, v) __builtin_amdgcn_raw_buffer_store_b128(v, rs, (int)((const char*)(p) - (const char*)(b0)), 0, 16)
;     __device__ __forceinline__ void operator()(const f32x4 (&acc)[2][2][4][2], const Unit& u, int wr, int wc, int fr, int fq) const {
;         const int row0 = u.pm * BM + wr * 64 + fr, col0 = u.pn * BM + wc * 32 + 8 * fq; const __amdgpu_buffer_rsrc_t rs_ = PG8_RSRC(out);
; #pragma unroll
;         for (int ai = 0; ai < 2; ++ai) {
;             f32x4 b0[4][2], b1[4][2];
; #pragma unroll
;             for (int m = 0; m < 4; ++m) { const size_t off = (size_t)(row0 + ai * HALF + m * 16) * ldc + col0;
; #pragma unroll
;                 for (int bj = 0; bj < 2; ++bj) {
;                     if (BASE_F32) { b0[m][bj] = *(const f32x4*)((const float*)base + off + bj * HALF); b1[m][bj] = *(const f32x4*)((const float*)base + off + bj * HALF + 4); }
;                     else { const u32x4 q = *(const u32x4*)((const bf16_t*)base + off + bj * HALF);
;                         b0[m][bj] = (f32x4){__uint_as_float(q.x << 16), __uint_as_float(q.x & 0xffff0000u), __uint_as_float(q.y << 16), __uint_as_float(q.y & 0xffff0000u)};
;                         b1[m][bj] = (f32x4){__uint_as_float(q.z << 16), __uint_as_float(q.z & 0xffff0000u), __uint_as_float(q.w << 16), __uint_as_float(q.w & 0xffff0000u)}; } } }
;             asm volatile("" ::: "memory");
; #pragma unroll
;             for (int m = 0; m < 4; ++m) { const size_t off = (size_t)(row0 + ai * HALF + m * 16) * ldc + col0; float ssq = 0.f;
; #pragma unroll
;                 for (int bj = 0; bj < 2; ++bj) {
;                     const f32x4 o0 = b0[m][bj] + acc[ai][bj][m][0] * sc, o1 = b1[m][bj] + acc[ai][bj][m][1] * sc;
;                     ssq += ((o0[0] * o0[0] + o0[1] * o0[1]) + (o0[2] * o0[2] + o0[3] * o0[3])) + ((o1[0] * o1[0] + o1[1] * o1[1]) + (o1[2] * o1[2] + o1[3] * o1[3]));
;                     u32x4 w; w.x = cvt_pk_bf16(o0[0], o0[1]); w.y = cvt_pk_bf16(o0[2], o0[3]); w.z = cvt_pk_bf16(o1[0], o1[1]); w.w = cvt_pk_bf16(o1[2], o1[3]);
;                     PG8_ST16(rs_, out, out + off + bj * HALF, w); }
;                 ssq += __shfl_xor(ssq, 16); ssq += __shfl_xor(ssq, 32);
;                 if (fq == 0) rowss[(size_t)(row0 + ai * HALF + m * 16) * 32 + 4 * u.pn + wc] = ssq; }
.LBB0_822:
	v_lshrrev_b32_e32 v252, 2, v215
	v_and_b32_e32 v207, 15, v215
	v_sub_u32_e32 v252, v252, v207
	v_lshlrev_b32_e32 v207, 4, v207
	v_lshrrev_b32_e32 v203, 4, v215
	v_lshl_or_b32 v207, v203, 2, v207
	v_and_b32_e32 v242, 3, v215
	v_sub_u32_e32 v203, v242, v203
	v_lshlrev_b32_e32 v204, 12, v252
	v_lshl_add_u32 v204, v203, 4, v204
	v_ashrrev_i32_e32 v205, 31, v204
	v_and_b32_e32 v203, 60, v215
	v_lshl_or_b32 v203, v242, 6, v203
	v_lshl_or_b32 v36, s70, 8, v188
	v_lshl_add_u32 v38, s71, 8, v186
	v_ashrrev_i32_e32 v37, 31, v36
	v_lshlrev_b64 v[192:193], 1, v[36:37]
	v_ashrrev_i32_e32 v39, 31, v38
	v_lshl_add_u64 v[40:41], s[20:21], 0, v[192:193]
	v_lshl_add_u64 v[40:41], v[40:41], 0, v[204:205]
	v_lshlrev_b64 v[190:191], 12, v[38:39]
	v_lshl_add_u64 v[4:5], v[40:41], 0, v[190:191]
	global_load_dwordx4 v[60:63], v[4:5], off
	global_load_dwordx4 v[76:79], v[4:5], off offset:256
	v_or_b32_e32 v54, 16, v38
	v_or_b32_e32 v52, 32, v38
	v_or_b32_e32 v42, 48, v38
	v_ashrrev_i32_e32 v55, 31, v54
	v_ashrrev_i32_e32 v53, 31, v52
	v_ashrrev_i32_e32 v43, 31, v42
	v_lshlrev_b64 v[4:5], 12, v[54:55]
	v_lshlrev_b64 v[6:7], 12, v[52:53]
	v_lshlrev_b64 v[8:9], 12, v[42:43]
	v_lshl_add_u64 v[4:5], v[40:41], 0, v[4:5]
	v_lshl_add_u64 v[6:7], v[40:41], 0, v[6:7]
	v_lshl_add_u64 v[194:195], v[40:41], 0, v[8:9]
	global_load_dwordx4 v[24:27], v[4:5], off
	global_load_dwordx4 v[20:23], v[4:5], off offset:256
	global_load_dwordx4 v[16:19], v[6:7], off
	global_load_dwordx4 v[12:15], v[6:7], off offset:256
	global_load_dwordx4 v[8:11], v[194:195], off
	s_nop 0
	global_load_dwordx4 v[4:7], v[194:195], off offset:256
	v_and_b32_e32 v195, 64, v215
	v_xor_b32_e32 v194, 16, v215
	v_add_u32_e32 v195, 64, v195
	v_xor_b32_e32 v196, 32, v215
	v_cmp_lt_i32_e32 vcc, v194, v195
	s_lshl_b32 s42, s70, 2
	s_ashr_i32 s43, s42, 31
	v_cndmask_b32_e32 v197, v215, v194, vcc
	v_cmp_lt_i32_e32 vcc, v196, v195
	v_lshl_add_u64 v[194:195], s[20:21], 0, v[190:191]
	v_lshlrev_b32_e32 v190, 2, v197
	v_cndmask_b32_e32 v202, v215, v196, vcc
	v_lshl_add_u64 v[192:193], v[194:195], 0, v[192:193]
	s_waitcnt vmcnt(0)
	ds_bpermute_b32 v60, v207, v60
	ds_bpermute_b32 v61, v207, v61
	ds_bpermute_b32 v62, v207, v62
	ds_bpermute_b32 v63, v207, v63
	ds_bpermute_b32 v76, v207, v76
	ds_bpermute_b32 v77, v207, v77
	ds_bpermute_b32 v78, v207, v78
	ds_bpermute_b32 v79, v207, v79
	ds_bpermute_b32 v24, v207, v24
	ds_bpermute_b32 v25, v207, v25
	ds_bpermute_b32 v26, v207, v26
	ds_bpermute_b32 v27, v207, v27
	ds_bpermute_b32 v20, v207, v20
	ds_bpermute_b32 v21, v207, v21
	ds_bpermute_b32 v22, v207, v22
	ds_bpermute_b32 v23, v207, v23
	ds_bpermute_b32 v16, v207, v16
	ds_bpermute_b32 v17, v207, v17
	ds_bpermute_b32 v18, v207, v18
	ds_bpermute_b32 v19, v207, v19
	ds_bpermute_b32 v12, v207, v12
	ds_bpermute_b32 v13, v207, v13
	ds_bpermute_b32 v14, v207, v14
	ds_bpermute_b32 v15, v207, v15
	ds_bpermute_b32 v8, v207, v8
	ds_bpermute_b32 v9, v207, v9
	ds_bpermute_b32 v10, v207, v10
	ds_bpermute_b32 v11, v207, v11
	ds_bpermute_b32 v4, v207, v4
	ds_bpermute_b32 v5, v207, v5
	ds_bpermute_b32 v6, v207, v6
	ds_bpermute_b32 v7, v207, v7
	s_waitcnt lgkmcnt(0)
	v_lshlrev_b32_e32 v194, 16, v60
	v_and_b32_e32 v195, 0xffff0000, v60
	v_lshlrev_b32_e32 v60, 16, v61
	v_and_b32_e32 v61, 0xffff0000, v61
	v_lshlrev_b32_e32 v196, 16, v62
	v_and_b32_e32 v197, 0xffff0000, v62
	v_lshlrev_b32_e32 v62, 16, v63
	v_and_b32_e32 v63, 0xffff0000, v63
	v_lshlrev_b32_e32 v198, 16, v76
	v_and_b32_e32 v199, 0xffff0000, v76
	v_lshlrev_b32_e32 v76, 16, v77
	v_and_b32_e32 v77, 0xffff0000, v77
	v_lshlrev_b32_e32 v200, 16, v78
	v_and_b32_e32 v201, 0xffff0000, v78
	v_lshlrev_b32_e32 v78, 16, v79
	v_and_b32_e32 v79, 0xffff0000, v79
	v_pk_add_f32 v[162:163], v[162:163], v[60:61]
	v_pk_add_f32 v[160:161], v[160:161], v[194:195]
	v_pk_add_f32 v[174:175], v[174:175], v[62:63]
	v_pk_add_f32 v[62:63], v[176:177], v[196:197]
	v_pk_add_f32 v[176:177], v[178:179], v[76:77]
	v_pk_add_f32 v[76:77], v[180:181], v[198:199]
	v_pk_add_f32 v[178:179], v[182:183], v[78:79]
	v_pk_add_f32 v[78:79], v[184:185], v[200:201]
	v_mul_f32_e32 v180, v161, v161
	v_mul_f32_e32 v181, v163, v163
	v_mul_f32_e32 v182, v63, v63
	v_mul_f32_e32 v183, v175, v175
	v_cvt_pk_bf16_f32 v60, v160, v161
	v_cvt_pk_bf16_f32 v61, v162, v163
	v_mul_f32_e32 v161, v77, v77
	v_mul_f32_e32 v163, v177, v177
	v_mul_f32_e32 v184, v79, v79
	v_mul_f32_e32 v185, v179, v179
	v_fmac_f32_e32 v180, v160, v160
	v_fmac_f32_e32 v181, v162, v162
	v_fmac_f32_e32 v182, v62, v62
	v_fmac_f32_e32 v183, v174, v174
	v_fmac_f32_e32 v161, v76, v76
	v_fmac_f32_e32 v163, v176, v176
	v_fmac_f32_e32 v184, v78, v78
	v_fmac_f32_e32 v185, v178, v178
	v_add_f32_e32 v160, v180, v181
	v_add_f32_e32 v162, v182, v183
	v_add_f32_e32 v161, v161, v163
	v_add_f32_e32 v163, v184, v185
	v_add_f32_e32 v160, v160, v162
	v_add_f32_e32 v161, v161, v163
	v_add_f32_e32 v160, v160, v161
	ds_bpermute_b32 v161, v190, v160
	v_cvt_pk_bf16_f32 v62, v62, v63
	v_cvt_pk_bf16_f32 v63, v174, v175
	v_lshl_add_u64 v[208:209], v[192:193], 0, v[204:205]
	ds_bpermute_b32 v242, v203, v60
	ds_bpermute_b32 v243, v203, v61
	ds_bpermute_b32 v244, v203, v62
	ds_bpermute_b32 v245, v203, v63
	v_cvt_pk_bf16_f32 v76, v76, v77
	v_cvt_pk_bf16_f32 v77, v176, v177
	v_cvt_pk_bf16_f32 v78, v78, v79
	v_cvt_pk_bf16_f32 v79, v178, v179
	s_waitcnt lgkmcnt(0)
	global_store_dwordx4 v[208:209], v[242:245], off
	ds_bpermute_b32 v246, v203, v76
	ds_bpermute_b32 v247, v203, v77
	ds_bpermute_b32 v248, v203, v78
	ds_bpermute_b32 v249, v203, v79
	s_waitcnt lgkmcnt(0)
	v_add_f32_e32 v60, v160, v161
	v_lshlrev_b32_e32 v160, 2, v202
	ds_bpermute_b32 v61, v160, v60
	s_and_saveexec_b64 s[44:45], s[36:37]
	s_cbranch_execz .LBB0_824
	v_lshlrev_b64 v[62:63], 7, v[38:39]
	v_lshl_add_u64 v[62:63], s[22:23], 0, v[62:63]
	v_lshl_add_u64 v[62:63], s[42:43], 2, v[62:63]
	s_lshl_b32 s46, s62, 2
	s_mov_b32 s47, s31
	v_lshl_add_u64 v[62:63], v[62:63], 0, s[46:47]
	s_waitcnt lgkmcnt(0)
	v_add_f32_e32 v39, v60, v61
	global_store_dword v[62:63], v39, off
; #define PG8_ST16(rs, b0, p, v) __builtin_amdgcn_raw_buffer_store_b128(v, rs, (int)((const char*)(p) - (const char*)(b0)), 0, 16)
; __device__ __forceinline__ unsigned cvt_pk_bf16(float lo, float hi) { unsigned r; asm volatile("v_cvt_pk_bf16_f32 %0, %1, %2" : "=v"(r) : "v"(lo), "v"(hi)); return r; }
;     __device__ __forceinline__ void operator()(const f32x4 (&acc)[2][2][4][2], const Unit& u, int wr, int wc, int fr, int fq) const {
;     ...
;                     else { const u32x4 q = *(const u32x4*)((const bf16_t*)base + off + bj * HALF);
;                         b0[m][bj] = (f32x4){__uint_as_float(q.x << 16), __uint_as_float(q.x & 0xffff0000u), __uint_as_float(q.y << 16), __uint_as_float(q.y & 0xffff0000u)};
;                         b1[m][bj] = (f32x4){__uint_as_float(q.z << 16), __uint_as_float(q.z & 0xffff0000u), __uint_as_float(q.w << 16), __uint_as_float(q.w & 0xffff0000u)}; } } }
;             asm volatile("" ::: "memory");
; #pragma unroll
;             for (int m = 0; m < 4; ++m) { const size_t off = (size_t)(row0 + ai * HALF + m * 16) * ldc + col0; float ssq = 0.f;
; #pragma unroll
;                 for (int bj = 0; bj < 2; ++bj) {
;                     const f32x4 o0 = b0[m][bj] + acc[ai][bj][m][0] * sc, o1 = b1[m][bj] + acc[ai][bj][m][1] * sc;
;                     ssq += ((o0[0] * o0[0] + o0[1] * o0[1]) + (o0[2] * o0[2] + o0[3] * o0[3])) + ((o1[0] * o1[0] + o1[1] * o1[1]) + (o1[2] * o1[2] + o1[3] * o1[3]));
;                     u32x4 w; w.x = cvt_pk_bf16(o0[0], o0[1]); w.y = cvt_pk_bf16(o0[2], o0[3]); w.z = cvt_pk_bf16(o1[0], o1[1]); w.w = cvt_pk_bf16(o1[2], o1[3]);
;                     PG8_ST16(rs_, out, out + off + bj * HALF, w); }
;                 ssq += __shfl_xor(ssq, 16); ssq += __shfl_xor(ssq, 32);
;                 if (fq == 0) rowss[(size_t)(row0 + ai * HALF + m * 16) * 32 + 4 * u.pn + wc] = ssq; }
.LBB0_824:
	s_or_b64 exec, exec, s[44:45]
	v_lshlrev_b32_e32 v62, 16, v24
	v_and_b32_e32 v63, 0xffff0000, v24
	v_lshlrev_b32_e32 v24, 16, v25
	v_and_b32_e32 v25, 0xffff0000, v25
	v_lshlrev_b32_e32 v78, 16, v20
	v_and_b32_e32 v79, 0xffff0000, v20
	v_lshlrev_b32_e32 v162, 16, v21
	v_and_b32_e32 v163, 0xffff0000, v21
	v_lshlrev_b32_e32 v174, 16, v22
	v_and_b32_e32 v175, 0xffff0000, v22
	v_lshlrev_b32_e32 v176, 16, v23
	v_and_b32_e32 v177, 0xffff0000, v23
	v_pk_add_f32 v[22:23], v[158:159], v[24:25]
	v_pk_add_f32 v[20:21], v[156:157], v[62:63]
	v_lshlrev_b32_e32 v76, 16, v26
	v_and_b32_e32 v77, 0xffff0000, v26
	v_lshlrev_b32_e32 v26, 16, v27
	v_and_b32_e32 v27, 0xffff0000, v27
	v_mul_f32_e32 v39, v21, v21
	v_mul_f32_e32 v62, v23, v23
	v_pk_add_f32 v[24:25], v[154:155], v[26:27]
	v_pk_add_f32 v[26:27], v[152:153], v[76:77]
	v_fmac_f32_e32 v39, v20, v20
	v_fmac_f32_e32 v62, v22, v22
	v_add_f32_e32 v39, v39, v62
	v_mul_f32_e32 v62, v27, v27
	v_mul_f32_e32 v63, v25, v25
	v_fmac_f32_e32 v62, v26, v26
	v_fmac_f32_e32 v63, v24, v24
	v_cvt_pk_bf16_f32 v20, v20, v21
	v_cvt_pk_bf16_f32 v21, v22, v23
	v_cvt_pk_bf16_f32 v22, v26, v27
	v_cvt_pk_bf16_f32 v23, v24, v25
	v_pk_add_f32 v[24:25], v[150:151], v[162:163]
	v_pk_add_f32 v[26:27], v[148:149], v[78:79]
	v_add_f32_e32 v62, v62, v63
	v_mul_f32_e32 v78, v27, v27
	v_mul_f32_e32 v79, v25, v25
	v_add_f32_e32 v39, v39, v62
	v_pk_add_f32 v[62:63], v[146:147], v[176:177]
	v_pk_add_f32 v[76:77], v[144:145], v[174:175]
	v_fmac_f32_e32 v78, v26, v26
	v_fmac_f32_e32 v79, v24, v24
	v_add_f32_e32 v78, v78, v79
	v_mul_f32_e32 v79, v77, v77
	v_mul_f32_e32 v144, v63, v63
	v_fmac_f32_e32 v79, v76, v76
	v_fmac_f32_e32 v144, v62, v62
	v_add_f32_e32 v79, v79, v144
	v_add_f32_e32 v78, v78, v79
	v_add_f32_e32 v39, v39, v78
	ds_bpermute_b32 v78, v190, v39
	s_waitcnt lgkmcnt(1)
	v_lshlrev_b64 v[60:61], 11, v[54:55]
	v_lshl_add_u64 v[60:61], v[60:61], 1, s[20:21]
	v_lshl_add_u64 v[60:61], v[36:37], 1, v[60:61]
	s_waitcnt lgkmcnt(0)
	global_store_dwordx4 v[208:209], v[246:249], off offset:256
	v_lshl_add_u64 v[208:209], v[60:61], 0, v[204:205]
	ds_bpermute_b32 v242, v203, v20
	ds_bpermute_b32 v243, v203, v21
	ds_bpermute_b32 v244, v203, v22
	ds_bpermute_b32 v245, v203, v23
	s_waitcnt lgkmcnt(0)
	s_nop 0
	v_add_f32_e32 v20, v39, v78
	ds_bpermute_b32 v21, v160, v20
	v_cvt_pk_bf16_f32 v22, v26, v27
	v_cvt_pk_bf16_f32 v23, v24, v25
	v_cvt_pk_bf16_f32 v24, v76, v77
	v_cvt_pk_bf16_f32 v25, v62, v63
	s_waitcnt lgkmcnt(0)
	global_store_dwordx4 v[208:209], v[242:245], off
	ds_bpermute_b32 v246, v203, v22
	ds_bpermute_b32 v247, v203, v23
	ds_bpermute_b32 v248, v203, v24
	ds_bpermute_b32 v249, v203, v25
	s_and_saveexec_b64 s[44:45], s[36:37]
	s_cbranch_execz .LBB0_826
	v_lshlrev_b64 v[22:23], 7, v[54:55]
	v_lshl_add_u64 v[22:23], s[22:23], 0, v[22:23]
	v_lshl_add_u64 v[22:23], s[42:43], 2, v[22:23]
	s_lshl_b32 s46, s62, 2
	s_mov_b32 s47, s31
	v_lshl_add_u64 v[22:23], v[22:23], 0, s[46:47]
	s_waitcnt lgkmcnt(0)
	v_add_f32_e32 v20, v20, v21
	global_store_dword v[22:23], v20, off
.LBB0_826:
	s_or_b64 exec, exec, s[44:45]
	v_lshlrev_b32_e32 v22, 16, v16
	v_and_b32_e32 v23, 0xffff0000, v16
	v_lshlrev_b32_e32 v16, 16, v17
	v_and_b32_e32 v17, 0xffff0000, v17
	v_lshlrev_b32_e32 v26, 16, v12
	v_and_b32_e32 v27, 0xffff0000, v12
	v_lshlrev_b32_e32 v54, 16, v13
	v_and_b32_e32 v55, 0xffff0000, v13
	v_lshlrev_b32_e32 v60, 16, v14
	v_and_b32_e32 v61, 0xffff0000, v14
	v_lshlrev_b32_e32 v62, 16, v15
	v_and_b32_e32 v63, 0xffff0000, v15
	v_pk_add_f32 v[14:15], v[142:143], v[16:17]
	v_pk_add_f32 v[12:13], v[140:141], v[22:23]
	v_lshlrev_b32_e32 v24, 16, v18
	v_and_b32_e32 v25, 0xffff0000, v18
	v_lshlrev_b32_e32 v18, 16, v19
	v_and_b32_e32 v19, 0xffff0000, v19
	v_mul_f32_e32 v22, v13, v13
	v_mul_f32_e32 v23, v15, v15
	v_pk_add_f32 v[16:17], v[138:139], v[18:19]
	v_pk_add_f32 v[18:19], v[136:137], v[24:25]
	v_fmac_f32_e32 v22, v12, v12
	v_fmac_f32_e32 v23, v14, v14
	v_add_f32_e32 v22, v22, v23
	v_mul_f32_e32 v23, v19, v19
	v_mul_f32_e32 v24, v17, v17
	v_fmac_f32_e32 v23, v18, v18
	v_fmac_f32_e32 v24, v16, v16
	v_cvt_pk_bf16_f32 v12, v12, v13
	v_cvt_pk_bf16_f32 v13, v14, v15
	v_cvt_pk_bf16_f32 v14, v18, v19
	v_cvt_pk_bf16_f32 v15, v16, v17
	v_pk_add_f32 v[16:17], v[134:135], v[54:55]
	v_pk_add_f32 v[18:19], v[132:133], v[26:27]
	v_add_f32_e32 v23, v23, v24
	v_mul_f32_e32 v26, v19, v19
	v_mul_f32_e32 v27, v17, v17
	v_add_f32_e32 v39, v22, v23
	v_pk_add_f32 v[22:23], v[130:131], v[62:63]
	v_pk_add_f32 v[24:25], v[128:129], v[60:61]
	v_fmac_f32_e32 v26, v18, v18
	v_fmac_f32_e32 v27, v16, v16
	v_add_f32_e32 v26, v26, v27
	v_mul_f32_e32 v27, v25, v25
	v_mul_f32_e32 v54, v23, v23
	v_fmac_f32_e32 v27, v24, v24
	v_fmac_f32_e32 v54, v22, v22
	v_add_f32_e32 v27, v27, v54
	v_add_f32_e32 v26, v26, v27
	v_add_f32_e32 v26, v39, v26
	ds_bpermute_b32 v27, v190, v26
	s_waitcnt lgkmcnt(1)
	v_lshlrev_b64 v[20:21], 11, v[52:53]
	v_lshl_add_u64 v[20:21], v[20:21], 1, s[20:21]
	v_lshl_add_u64 v[20:21], v[36:37], 1, v[20:21]
	s_waitcnt lgkmcnt(0)
	global_store_dwordx4 v[208:209], v[246:249], off offset:256
	v_lshl_add_u64 v[208:209], v[20:21], 0, v[204:205]
	ds_bpermute_b32 v242, v203, v12
	ds_bpermute_b32 v243, v203, v13
	ds_bpermute_b32 v244, v203, v14
	ds_bpermute_b32 v245, v203, v15
	s_waitcnt lgkmcnt(0)
	s_nop 0
	v_add_f32_e32 v12, v26, v27
	ds_bpermute_b32 v13, v160, v12
	v_cvt_pk_bf16_f32 v14, v18, v19
	v_cvt_pk_bf16_f32 v15, v16, v17
	v_cvt_pk_bf16_f32 v16, v24, v25
	v_cvt_pk_bf16_f32 v17, v22, v23
	s_waitcnt lgkmcnt(0)
	global_store_dwordx4 v[208:209], v[242:245], off
	ds_bpermute_b32 v246, v203, v14
	ds_bpermute_b32 v247, v203, v15
	ds_bpermute_b32 v248, v203, v16
	ds_bpermute_b32 v249, v203, v17
	s_and_saveexec_b64 s[44:45], s[36:37]
	s_cbranch_execz .LBB0_828
	v_lshlrev_b64 v[14:15], 7, v[52:53]
	v_lshl_add_u64 v[14:15], s[22:23], 0, v[14:15]
	v_lshl_add_u64 v[14:15], s[42:43], 2, v[14:15]
	s_lshl_b32 s46, s62, 2
	s_mov_b32 s47, s31
	v_lshl_add_u64 v[14:15], v[14:15], 0, s[46:47]
	s_waitcnt lgkmcnt(0)
	v_add_f32_e32 v12, v12, v13
	global_store_dword v[14:15], v12, off
; #define PG8_ST16(rs, b0, p, v) __builtin_amdgcn_raw_buffer_store_b128(v, rs, (int)((const char*)(p) - (const char*)(b0)), 0, 16)
; __device__ __forceinline__ unsigned cvt_pk_bf16(float lo, float hi) { unsigned r; asm volatile("v_cvt_pk_bf16_f32 %0, %1, %2" : "=v"(r) : "v"(lo), "v"(hi)); return r; }
;     __device__ __forceinline__ void operator()(const f32x4 (&acc)[2][2][4][2], const Unit& u, int wr, int wc, int fr, int fq) const {
;     ...
;             for (int m = 0; m < 4; ++m) { const size_t off = (size_t)(row0 + ai * HALF + m * 16) * ldc + col0;
; #pragma unroll
;                 for (int bj = 0; bj < 2; ++bj) {
;                     if (BASE_F32) { b0[m][bj] = *(const f32x4*)((const float*)base + off + bj * HALF); b1[m][bj] = *(const f32x4*)((const float*)base + off + bj * HALF + 4); }
;                     else { const u32x4 q = *(const u32x4*)((const bf16_t*)base + off + bj * HALF);
;                         b0[m][bj] = (f32x4){__uint_as_float(q.x << 16), __uint_as_float(q.x & 0xffff0000u), __uint_as_float(q.y << 16), __uint_as_float(q.y & 0xffff0000u)};
;                         b1[m][bj] = (f32x4){__uint_as_float(q.z << 16), __uint_as_float(q.z & 0xffff0000u), __uint_as_float(q.w << 16), __uint_as_float(q.w & 0xffff0000u)}; } } }
;             asm volatile("" ::: "memory");
; #pragma unroll
;             for (int m = 0; m < 4; ++m) { const size_t off = (size_t)(row0 + ai * HALF + m * 16) * ldc + col0; float ssq = 0.f;
; #pragma unroll
;                 for (int bj = 0; bj < 2; ++bj) {
;                     const f32x4 o0 = b0[m][bj] + acc[ai][bj][m][0] * sc, o1 = b1[m][bj] + acc[ai][bj][m][1] * sc;
;                     ssq += ((o0[0] * o0[0] + o0[1] * o0[1]) + (o0[2] * o0[2] + o0[3] * o0[3])) + ((o1[0] * o1[0] + o1[1] * o1[1]) + (o1[2] * o1[2] + o1[3] * o1[3]));
;                     u32x4 w; w.x = cvt_pk_bf16(o0[0], o0[1]); w.y = cvt_pk_bf16(o0[2], o0[3]); w.z = cvt_pk_bf16(o1[0], o1[1]); w.w = cvt_pk_bf16(o1[2], o1[3]);
;                     PG8_ST16(rs_, out, out + off + bj * HALF, w); }
;                 ssq += __shfl_xor(ssq, 16); ssq += __shfl_xor(ssq, 32);
;                 if (fq == 0) rowss[(size_t)(row0 + ai * HALF + m * 16) * 32 + 4 * u.pn + wc] = ssq; }
.LBB0_828:
	s_or_b64 exec, exec, s[44:45]
	v_lshlrev_b32_e32 v14, 16, v8
	v_and_b32_e32 v15, 0xffff0000, v8
	v_lshlrev_b32_e32 v8, 16, v9
	v_and_b32_e32 v9, 0xffff0000, v9
	v_lshlrev_b32_e32 v18, 16, v4
	v_and_b32_e32 v19, 0xffff0000, v4
	v_lshlrev_b32_e32 v20, 16, v5
	v_and_b32_e32 v21, 0xffff0000, v5
	v_lshlrev_b32_e32 v22, 16, v6
	v_and_b32_e32 v23, 0xffff0000, v6
	v_lshlrev_b32_e32 v24, 16, v7
	v_and_b32_e32 v25, 0xffff0000, v7
	v_pk_add_f32 v[6:7], v[126:127], v[8:9]
	v_pk_add_f32 v[4:5], v[124:125], v[14:15]
	v_lshlrev_b32_e32 v16, 16, v10
	v_and_b32_e32 v17, 0xffff0000, v10
	v_lshlrev_b32_e32 v10, 16, v11
	v_and_b32_e32 v11, 0xffff0000, v11
	v_mul_f32_e32 v14, v5, v5
	v_mul_f32_e32 v15, v7, v7
	v_pk_add_f32 v[8:9], v[122:123], v[10:11]
	v_pk_add_f32 v[10:11], v[120:121], v[16:17]
	v_fmac_f32_e32 v14, v4, v4
	v_fmac_f32_e32 v15, v6, v6
	v_add_f32_e32 v14, v14, v15
	v_mul_f32_e32 v15, v11, v11
	v_mul_f32_e32 v16, v9, v9
	v_fmac_f32_e32 v15, v10, v10
	v_fmac_f32_e32 v16, v8, v8
	v_cvt_pk_bf16_f32 v4, v4, v5
	v_cvt_pk_bf16_f32 v5, v6, v7
	v_cvt_pk_bf16_f32 v6, v10, v11
	v_cvt_pk_bf16_f32 v7, v8, v9
	v_pk_add_f32 v[8:9], v[118:119], v[20:21]
	v_pk_add_f32 v[10:11], v[116:117], v[18:19]
	v_add_f32_e32 v15, v15, v16
	v_mul_f32_e32 v18, v11, v11
	v_mul_f32_e32 v19, v9, v9
	v_add_f32_e32 v26, v14, v15
	v_pk_add_f32 v[14:15], v[114:115], v[24:25]
	v_pk_add_f32 v[16:17], v[112:113], v[22:23]
	v_fmac_f32_e32 v18, v10, v10
	v_fmac_f32_e32 v19, v8, v8
	v_add_f32_e32 v18, v18, v19
	v_mul_f32_e32 v19, v17, v17
	v_mul_f32_e32 v20, v15, v15
	v_fmac_f32_e32 v19, v16, v16
	v_fmac_f32_e32 v20, v14, v14
	v_add_f32_e32 v19, v19, v20
	v_add_f32_e32 v18, v18, v19
	v_add_f32_e32 v18, v26, v18
	ds_bpermute_b32 v19, v190, v18
	s_waitcnt lgkmcnt(1)
	v_lshlrev_b64 v[12:13], 11, v[42:43]
	v_lshl_add_u64 v[12:13], v[12:13], 1, s[20:21]
	v_lshl_add_u64 v[12:13], v[36:37], 1, v[12:13]
	s_waitcnt lgkmcnt(0)
	global_store_dwordx4 v[208:209], v[246:249], off offset:256
	v_lshl_add_u64 v[208:209], v[12:13], 0, v[204:205]
	ds_bpermute_b32 v242, v203, v4
	ds_bpermute_b32 v243, v203, v5
	ds_bpermute_b32 v244, v203, v6
	ds_bpermute_b32 v245, v203, v7
	s_waitcnt lgkmcnt(0)
	s_nop 0
	v_add_f32_e32 v4, v18, v19
	ds_bpermute_b32 v5, v160, v4
	v_cvt_pk_bf16_f32 v6, v10, v11
	v_cvt_pk_bf16_f32 v7, v8, v9
	v_cvt_pk_bf16_f32 v8, v16, v17
	v_cvt_pk_bf16_f32 v9, v14, v15
	s_waitcnt lgkmcnt(0)
	global_store_dwordx4 v[208:209], v[242:245], off
	ds_bpermute_b32 v246, v203, v6
	ds_bpermute_b32 v247, v203, v7
	ds_bpermute_b32 v248, v203, v8
	ds_bpermute_b32 v249, v203, v9
	s_waitcnt lgkmcnt(0)
	global_store_dwordx4 v[208:209], v[246:249], off offset:256
	s_and_saveexec_b64 s[44:45], s[36:37]
	s_cbranch_execz .LBB0_830
	v_lshlrev_b64 v[6:7], 7, v[42:43]
	v_lshl_add_u64 v[6:7], s[22:23], 0, v[6:7]
	v_lshl_add_u64 v[6:7], s[42:43], 2, v[6:7]
	s_lshl_b32 s46, s62, 2
	s_mov_b32 s47, s31
	v_lshl_add_u64 v[6:7], v[6:7], 0, s[46:47]
	s_waitcnt lgkmcnt(0)
	v_add_f32_e32 v4, v4, v5
	global_store_dword v[6:7], v4, off
.LBB0_830:
	s_or_b64 exec, exec, s[44:45]
	v_add_u32_e32 v54, 0x80, v38
	v_ashrrev_i32_e32 v55, 31, v54
	v_lshlrev_b64 v[112:113], 12, v[54:55]
	v_lshl_add_u64 v[8:9], v[40:41], 0, v[112:113]
	s_waitcnt lgkmcnt(0)
	global_load_dwordx4 v[222:225], v[8:9], off
	global_load_dwordx4 v[218:221], v[8:9], off offset:256
	v_add_u32_e32 v52, 0x90, v38
	v_ashrrev_i32_e32 v53, 31, v52
	v_add_u32_e32 v42, 0xa0, v38
	v_ashrrev_i32_e32 v43, 31, v42
	v_add_u32_e32 v38, 0xb0, v38
	v_ashrrev_i32_e32 v39, 31, v38
	v_lshlrev_b64 v[4:5], 12, v[52:53]
	v_lshl_add_u64 v[4:5], v[40:41], 0, v[4:5]
	global_load_dwordx4 v[24:27], v[4:5], off
	global_load_dwordx4 v[20:23], v[4:5], off offset:256
	v_lshlrev_b64 v[4:5], 12, v[42:43]
	v_lshl_add_u64 v[4:5], v[40:41], 0, v[4:5]
	global_load_dwordx4 v[16:19], v[4:5], off
	global_load_dwordx4 v[12:15], v[4:5], off offset:256
	v_lshlrev_b64 v[4:5], 12, v[38:39]
	v_lshl_add_u64 v[4:5], v[40:41], 0, v[4:5]
	global_load_dwordx4 v[8:11], v[4:5], off
	s_nop 0
	global_load_dwordx4 v[4:7], v[4:5], off offset:256
	s_waitcnt vmcnt(0)
	ds_bpermute_b32 v222, v207, v222
	ds_bpermute_b32 v223, v207, v223
	ds_bpermute_b32 v224, v207, v224
	ds_bpermute_b32 v225, v207, v225
	ds_bpermute_b32 v218, v207, v218
	ds_bpermute_b32 v219, v207, v219
	ds_bpermute_b32 v220, v207, v220
	ds_bpermute_b32 v221, v207, v221
	ds_bpermute_b32 v24, v207, v24
	ds_bpermute_b32 v25, v207, v25
	ds_bpermute_b32 v26, v207, v26
	ds_bpermute_b32 v27, v207, v27
	ds_bpermute_b32 v20, v207, v20
	ds_bpermute_b32 v21, v207, v21
	ds_bpermute_b32 v22, v207, v22
	ds_bpermute_b32 v23, v207, v23
	ds_bpermute_b32 v16, v207, v16
	ds_bpermute_b32 v17, v207, v17
	ds_bpermute_b32 v18, v207, v18
	ds_bpermute_b32 v19, v207, v19
	ds_bpermute_b32 v12, v207, v12
	ds_bpermute_b32 v13, v207, v13
	ds_bpermute_b32 v14, v207, v14
	ds_bpermute_b32 v15, v207, v15
	ds_bpermute_b32 v8, v207, v8
	ds_bpermute_b32 v9, v207, v9
	ds_bpermute_b32 v10, v207, v10
	ds_bpermute_b32 v11, v207, v11
	ds_bpermute_b32 v4, v207, v4
	ds_bpermute_b32 v5, v207, v5
	ds_bpermute_b32 v6, v207, v6
	ds_bpermute_b32 v7, v207, v7
	s_waitcnt lgkmcnt(0)
; #define PG8_ST16(rs, b0, p, v) __builtin_amdgcn_raw_buffer_store_b128(v, rs, (int)((const char*)(p) - (const char*)(b0)), 0, 16)
; __device__ __forceinline__ unsigned cvt_pk_bf16(float lo, float hi) { unsigned r; asm volatile("v_cvt_pk_bf16_f32 %0, %1, %2" : "=v"(r) : "v"(lo), "v"(hi)); return r; }
;     __device__ __forceinline__ void operator()(const f32x4 (&acc)[2][2][4][2], const Unit& u, int wr, int wc, int fr, int fq) const {
;     ...
;             for (int m = 0; m < 4; ++m) { const size_t off = (size_t)(row0 + ai * HALF + m * 16) * ldc + col0; float ssq = 0.f;
; #pragma unroll
;                 for (int bj = 0; bj < 2; ++bj) {
;                     const f32x4 o0 = b0[m][bj] + acc[ai][bj][m][0] * sc, o1 = b1[m][bj] + acc[ai][bj][m][1] * sc;
;                     ssq += ((o0[0] * o0[0] + o0[1] * o0[1]) + (o0[2] * o0[2] + o0[3] * o0[3])) + ((o1[0] * o1[0] + o1[1] * o1[1]) + (o1[2] * o1[2] + o1[3] * o1[3]));
;                     u32x4 w; w.x = cvt_pk_bf16(o0[0], o0[1]); w.y = cvt_pk_bf16(o0[2], o0[3]); w.z = cvt_pk_bf16(o1[0], o1[1]); w.w = cvt_pk_bf16(o1[2], o1[3]);
;                     PG8_ST16(rs_, out, out + off + bj * HALF, w); }
;                 ssq += __shfl_xor(ssq, 16); ssq += __shfl_xor(ssq, 32);
;                 if (fq == 0) rowss[(size_t)(row0 + ai * HALF + m * 16) * 32 + 4 * u.pn + wc] = ssq; }
	v_lshlrev_b32_e32 v116, 16, v222
	v_and_b32_e32 v117, 0xffff0000, v222
	v_lshlrev_b32_e32 v120, 16, v223
	v_and_b32_e32 v121, 0xffff0000, v223
	v_lshlrev_b32_e32 v114, 16, v224
	v_and_b32_e32 v115, 0xffff0000, v224
	v_lshlrev_b32_e32 v118, 16, v225
	v_and_b32_e32 v119, 0xffff0000, v225
	v_pk_add_f32 v[108:109], v[108:109], v[116:117]
	v_lshlrev_b32_e32 v62, 16, v218
	v_and_b32_e32 v63, 0xffff0000, v218
	v_lshlrev_b32_e32 v78, 16, v219
	v_and_b32_e32 v79, 0xffff0000, v219
	v_lshlrev_b32_e32 v60, 16, v220
	v_and_b32_e32 v61, 0xffff0000, v220
	v_lshlrev_b32_e32 v76, 16, v221
	v_and_b32_e32 v77, 0xffff0000, v221
	v_pk_add_f32 v[40:41], v[110:111], v[120:121]
	v_pk_add_f32 v[78:79], v[102:103], v[78:79]
	v_pk_add_f32 v[62:63], v[100:101], v[62:63]
	v_pk_add_f32 v[110:111], v[106:107], v[118:119]
	v_pk_add_f32 v[106:107], v[104:105], v[114:115]
	v_mul_f32_e32 v104, v109, v109
	v_mul_f32_e32 v105, v41, v41
	v_pk_add_f32 v[96:97], v[96:97], v[60:61]
	v_mul_f32_e32 v60, v63, v63
	v_mul_f32_e32 v61, v79, v79
	v_fmac_f32_e32 v104, v108, v108
	v_fmac_f32_e32 v105, v40, v40
	v_pk_add_f32 v[76:77], v[98:99], v[76:77]
	v_fmac_f32_e32 v60, v62, v62
	v_fmac_f32_e32 v61, v78, v78
	v_add_f32_e32 v104, v104, v105
	v_mul_f32_e32 v105, v107, v107
	v_mul_f32_e32 v114, v111, v111
	v_add_f32_e32 v60, v60, v61
	v_mul_f32_e32 v61, v97, v97
	v_mul_f32_e32 v98, v77, v77
	v_fmac_f32_e32 v105, v106, v106
	v_fmac_f32_e32 v114, v110, v110
	v_fmac_f32_e32 v61, v96, v96
	v_fmac_f32_e32 v98, v76, v76
	v_add_f32_e32 v105, v105, v114
	v_add_f32_e32 v61, v61, v98
	v_add_f32_e32 v114, v104, v105
	v_cvt_pk_bf16_f32 v104, v108, v109
	v_cvt_pk_bf16_f32 v105, v40, v41
	v_lshl_add_u64 v[40:41], s[20:21], 0, v[112:113]
	v_add_f32_e32 v60, v60, v61
	v_lshl_add_u64 v[40:41], v[36:37], 1, v[40:41]
	v_add_f32_e32 v98, v114, v60
	v_cvt_pk_bf16_f32 v106, v106, v107
	v_cvt_pk_bf16_f32 v107, v110, v111
	v_lshl_add_u64 v[208:209], v[40:41], 0, v[204:205]
	ds_bpermute_b32 v242, v203, v104
	ds_bpermute_b32 v243, v203, v105
	ds_bpermute_b32 v244, v203, v106
	ds_bpermute_b32 v245, v203, v107
	v_cvt_pk_bf16_f32 v60, v62, v63
	v_cvt_pk_bf16_f32 v61, v78, v79
	v_cvt_pk_bf16_f32 v62, v96, v97
	v_cvt_pk_bf16_f32 v63, v76, v77
	s_waitcnt lgkmcnt(0)
	global_store_dwordx4 v[208:209], v[242:245], off
	ds_bpermute_b32 v246, v203, v60
	ds_bpermute_b32 v247, v203, v61
	ds_bpermute_b32 v248, v203, v62
	ds_bpermute_b32 v249, v203, v63
	ds_bpermute_b32 v40, v190, v98
	s_waitcnt lgkmcnt(0)
	v_add_f32_e32 v40, v98, v40
	ds_bpermute_b32 v41, v160, v40
	s_and_saveexec_b64 s[44:45], s[36:37]
	s_cbranch_execz .LBB0_832
	v_lshlrev_b64 v[54:55], 7, v[54:55]
	v_lshl_add_u64 v[54:55], s[22:23], 0, v[54:55]
	v_lshl_add_u64 v[54:55], s[42:43], 2, v[54:55]
	s_lshl_b32 s46, s62, 2
	s_mov_b32 s47, s31
	v_lshl_add_u64 v[54:55], v[54:55], 0, s[46:47]
	s_waitcnt lgkmcnt(0)
	v_add_f32_e32 v40, v40, v41
	global_store_dword v[54:55], v40, off
.LBB0_832:
	s_or_b64 exec, exec, s[44:45]
	s_waitcnt vmcnt(7)
	v_lshlrev_b32_e32 v54, 16, v24
	v_and_b32_e32 v55, 0xffff0000, v24
	v_lshlrev_b32_e32 v24, 16, v25
	v_and_b32_e32 v25, 0xffff0000, v25
	s_waitcnt vmcnt(6)
	v_lshlrev_b32_e32 v62, 16, v20
	v_and_b32_e32 v63, 0xffff0000, v20
	v_lshlrev_b32_e32 v76, 16, v21
	v_and_b32_e32 v77, 0xffff0000, v21
	v_lshlrev_b32_e32 v78, 16, v22
	v_and_b32_e32 v79, 0xffff0000, v22
	v_lshlrev_b32_e32 v96, 16, v23
	v_and_b32_e32 v97, 0xffff0000, v23
	v_pk_add_f32 v[22:23], v[94:95], v[24:25]
	v_pk_add_f32 v[20:21], v[92:93], v[54:55]
	v_lshlrev_b32_e32 v60, 16, v26
	v_and_b32_e32 v61, 0xffff0000, v26
	v_lshlrev_b32_e32 v26, 16, v27
	v_and_b32_e32 v27, 0xffff0000, v27
	v_mul_f32_e32 v54, v21, v21
	v_mul_f32_e32 v55, v23, v23
	v_pk_add_f32 v[24:25], v[90:91], v[26:27]
	v_pk_add_f32 v[26:27], v[88:89], v[60:61]
	v_fmac_f32_e32 v54, v20, v20
	v_fmac_f32_e32 v55, v22, v22
	v_add_f32_e32 v54, v54, v55
	v_mul_f32_e32 v55, v27, v27
	v_mul_f32_e32 v60, v25, v25
	v_fmac_f32_e32 v55, v26, v26
	v_fmac_f32_e32 v60, v24, v24
	v_cvt_pk_bf16_f32 v20, v20, v21
	v_cvt_pk_bf16_f32 v21, v22, v23
	v_cvt_pk_bf16_f32 v22, v26, v27
	v_cvt_pk_bf16_f32 v23, v24, v25
	v_pk_add_f32 v[24:25], v[86:87], v[76:77]
	v_pk_add_f32 v[26:27], v[84:85], v[62:63]
	v_add_f32_e32 v55, v55, v60
	v_mul_f32_e32 v62, v27, v27
	v_mul_f32_e32 v63, v25, v25
	v_add_f32_e32 v88, v54, v55
	v_pk_add_f32 v[54:55], v[82:83], v[96:97]
	v_pk_add_f32 v[60:61], v[80:81], v[78:79]
	v_fmac_f32_e32 v62, v26, v26
	v_fmac_f32_e32 v63, v24, v24
	v_add_f32_e32 v62, v62, v63
	v_mul_f32_e32 v63, v61, v61
	v_mul_f32_e32 v76, v55, v55
	v_fmac_f32_e32 v63, v60, v60
	v_fmac_f32_e32 v76, v54, v54
	v_add_f32_e32 v63, v63, v76
	v_add_f32_e32 v62, v62, v63
	v_add_f32_e32 v62, v88, v62
	ds_bpermute_b32 v63, v190, v62
	s_waitcnt lgkmcnt(1)
	v_lshlrev_b64 v[40:41], 11, v[52:53]
	v_lshl_add_u64 v[40:41], v[40:41], 1, s[20:21]
	v_lshl_add_u64 v[40:41], v[36:37], 1, v[40:41]
	s_waitcnt lgkmcnt(0)
	global_store_dwordx4 v[208:209], v[246:249], off offset:256
	v_lshl_add_u64 v[208:209], v[40:41], 0, v[204:205]
	ds_bpermute_b32 v242, v203, v20
	ds_bpermute_b32 v243, v203, v21
	ds_bpermute_b32 v244, v203, v22
	ds_bpermute_b32 v245, v203, v23
	s_waitcnt lgkmcnt(0)
	s_nop 0
	v_add_f32_e32 v20, v62, v63
	ds_bpermute_b32 v21, v160, v20
	v_cvt_pk_bf16_f32 v22, v26, v27
	v_cvt_pk_bf16_f32 v23, v24, v25
	v_cvt_pk_bf16_f32 v24, v60, v61
	v_cvt_pk_bf16_f32 v25, v54, v55
	s_waitcnt lgkmcnt(0)
	global_store_dwordx4 v[208:209], v[242:245], off
	ds_bpermute_b32 v246, v203, v22
	ds_bpermute_b32 v247, v203, v23
	ds_bpermute_b32 v248, v203, v24
	ds_bpermute_b32 v249, v203, v25
	s_and_saveexec_b64 s[44:45], s[36:37]
	s_cbranch_execz .LBB0_834
	v_lshlrev_b64 v[22:23], 7, v[52:53]
	v_lshl_add_u64 v[22:23], s[22:23], 0, v[22:23]
	v_lshl_add_u64 v[22:23], s[42:43], 2, v[22:23]
	s_lshl_b32 s46, s62, 2
	s_mov_b32 s47, s31
	v_lshl_add_u64 v[22:23], v[22:23], 0, s[46:47]
	s_waitcnt lgkmcnt(0)
	v_add_f32_e32 v20, v20, v21
	global_store_dword v[22:23], v20, off
; #define PG8_ST16(rs, b0, p, v) __builtin_amdgcn_raw_buffer_store_b128(v, rs, (int)((const char*)(p) - (const char*)(b0)), 0, 16)
; __device__ __forceinline__ unsigned cvt_pk_bf16(float lo, float hi) { unsigned r; asm volatile("v_cvt_pk_bf16_f32 %0, %1, %2" : "=v"(r) : "v"(lo), "v"(hi)); return r; }
;     __device__ __forceinline__ void operator()(const f32x4 (&acc)[2][2][4][2], const Unit& u, int wr, int wc, int fr, int fq) const {
;     ...
;             for (int m = 0; m < 4; ++m) { const size_t off = (size_t)(row0 + ai * HALF + m * 16) * ldc + col0; float ssq = 0.f;
; #pragma unroll
;                 for (int bj = 0; bj < 2; ++bj) {
;                     const f32x4 o0 = b0[m][bj] + acc[ai][bj][m][0] * sc, o1 = b1[m][bj] + acc[ai][bj][m][1] * sc;
;                     ssq += ((o0[0] * o0[0] + o0[1] * o0[1]) + (o0[2] * o0[2] + o0[3] * o0[3])) + ((o1[0] * o1[0] + o1[1] * o1[1]) + (o1[2] * o1[2] + o1[3] * o1[3]));
;                     u32x4 w; w.x = cvt_pk_bf16(o0[0], o0[1]); w.y = cvt_pk_bf16(o0[2], o0[3]); w.z = cvt_pk_bf16(o1[0], o1[1]); w.w = cvt_pk_bf16(o1[2], o1[3]);
;                     PG8_ST16(rs_, out, out + off + bj * HALF, w); }
;                 ssq += __shfl_xor(ssq, 16); ssq += __shfl_xor(ssq, 32);
;                 if (fq == 0) rowss[(size_t)(row0 + ai * HALF + m * 16) * 32 + 4 * u.pn + wc] = ssq; }
.LBB0_834:
	s_or_b64 exec, exec, s[44:45]
	s_waitcnt vmcnt(7)
	v_lshlrev_b32_e32 v22, 16, v16
	v_and_b32_e32 v23, 0xffff0000, v16
	v_lshlrev_b32_e32 v16, 16, v17
	v_and_b32_e32 v17, 0xffff0000, v17
	s_waitcnt vmcnt(6)
	v_lshlrev_b32_e32 v26, 16, v12
	v_and_b32_e32 v27, 0xffff0000, v12
	v_lshlrev_b32_e32 v40, 16, v13
	v_and_b32_e32 v41, 0xffff0000, v13
	v_lshlrev_b32_e32 v52, 16, v14
	v_and_b32_e32 v53, 0xffff0000, v14
	v_lshlrev_b32_e32 v54, 16, v15
	v_and_b32_e32 v55, 0xffff0000, v15
	v_pk_add_f32 v[14:15], v[74:75], v[16:17]
	v_pk_add_f32 v[12:13], v[72:73], v[22:23]
	v_lshlrev_b32_e32 v24, 16, v18
	v_and_b32_e32 v25, 0xffff0000, v18
	v_lshlrev_b32_e32 v18, 16, v19
	v_and_b32_e32 v19, 0xffff0000, v19
	v_mul_f32_e32 v22, v13, v13
	v_mul_f32_e32 v23, v15, v15
	v_pk_add_f32 v[16:17], v[70:71], v[18:19]
	v_pk_add_f32 v[18:19], v[68:69], v[24:25]
	v_fmac_f32_e32 v22, v12, v12
	v_fmac_f32_e32 v23, v14, v14
	v_add_f32_e32 v22, v22, v23
	v_mul_f32_e32 v23, v19, v19
	v_mul_f32_e32 v24, v17, v17
	v_fmac_f32_e32 v23, v18, v18
	v_fmac_f32_e32 v24, v16, v16
	v_cvt_pk_bf16_f32 v12, v12, v13
	v_cvt_pk_bf16_f32 v13, v14, v15
	v_cvt_pk_bf16_f32 v14, v18, v19
	v_cvt_pk_bf16_f32 v15, v16, v17
	v_pk_add_f32 v[16:17], v[66:67], v[40:41]
	v_pk_add_f32 v[18:19], v[64:65], v[26:27]
	v_add_f32_e32 v23, v23, v24
	v_mul_f32_e32 v26, v19, v19
	v_mul_f32_e32 v27, v17, v17
	v_add_f32_e32 v60, v22, v23
	v_pk_add_f32 v[22:23], v[58:59], v[54:55]
	v_pk_add_f32 v[24:25], v[56:57], v[52:53]
	v_fmac_f32_e32 v26, v18, v18
	v_fmac_f32_e32 v27, v16, v16
	v_add_f32_e32 v26, v26, v27
	v_mul_f32_e32 v27, v25, v25
	v_mul_f32_e32 v40, v23, v23
	v_fmac_f32_e32 v27, v24, v24
	v_fmac_f32_e32 v40, v22, v22
	v_add_f32_e32 v27, v27, v40
	v_add_f32_e32 v26, v26, v27
	v_add_f32_e32 v26, v60, v26
	ds_bpermute_b32 v27, v190, v26
	s_waitcnt lgkmcnt(1)
	v_lshlrev_b64 v[20:21], 11, v[42:43]
	v_lshl_add_u64 v[20:21], v[20:21], 1, s[20:21]
	v_lshl_add_u64 v[20:21], v[36:37], 1, v[20:21]
	s_waitcnt lgkmcnt(0)
	global_store_dwordx4 v[208:209], v[246:249], off offset:256
	v_lshl_add_u64 v[208:209], v[20:21], 0, v[204:205]
	ds_bpermute_b32 v242, v203, v12
	ds_bpermute_b32 v243, v203, v13
	ds_bpermute_b32 v244, v203, v14
	ds_bpermute_b32 v245, v203, v15
	s_waitcnt lgkmcnt(0)
	s_nop 0
	v_add_f32_e32 v12, v26, v27
	ds_bpermute_b32 v13, v160, v12
	v_cvt_pk_bf16_f32 v14, v18, v19
	v_cvt_pk_bf16_f32 v15, v16, v17
	v_cvt_pk_bf16_f32 v16, v24, v25
	v_cvt_pk_bf16_f32 v17, v22, v23
	s_waitcnt lgkmcnt(0)
	global_store_dwordx4 v[208:209], v[242:245], off
	ds_bpermute_b32 v246, v203, v14
	ds_bpermute_b32 v247, v203, v15
	ds_bpermute_b32 v248, v203, v16
	ds_bpermute_b32 v249, v203, v17
	s_and_saveexec_b64 s[44:45], s[36:37]
	s_cbranch_execz .LBB0_836
	v_lshlrev_b64 v[14:15], 7, v[42:43]
	v_lshl_add_u64 v[14:15], s[22:23], 0, v[14:15]
	v_lshl_add_u64 v[14:15], s[42:43], 2, v[14:15]
	s_lshl_b32 s46, s62, 2
	s_mov_b32 s47, s31
	v_lshl_add_u64 v[14:15], v[14:15], 0, s[46:47]
	s_waitcnt lgkmcnt(0)
	v_add_f32_e32 v12, v12, v13
	global_store_dword v[14:15], v12, off
.LBB0_836:
	s_or_b64 exec, exec, s[44:45]
	s_waitcnt vmcnt(7)
	v_lshlrev_b32_e32 v14, 16, v8
	v_and_b32_e32 v15, 0xffff0000, v8
	v_lshlrev_b32_e32 v8, 16, v9
	v_and_b32_e32 v9, 0xffff0000, v9
	s_waitcnt vmcnt(6)
	v_lshlrev_b32_e32 v18, 16, v4
	v_and_b32_e32 v19, 0xffff0000, v4
	v_lshlrev_b32_e32 v20, 16, v5
	v_and_b32_e32 v21, 0xffff0000, v5
	v_lshlrev_b32_e32 v22, 16, v6
	v_and_b32_e32 v23, 0xffff0000, v6
	v_lshlrev_b32_e32 v24, 16, v7
	v_and_b32_e32 v25, 0xffff0000, v7
	v_pk_add_f32 v[6:7], v[50:51], v[8:9]
	v_pk_add_f32 v[4:5], v[48:49], v[14:15]
	v_lshlrev_b32_e32 v16, 16, v10
	v_and_b32_e32 v17, 0xffff0000, v10
	v_lshlrev_b32_e32 v10, 16, v11
	v_and_b32_e32 v11, 0xffff0000, v11
	v_mul_f32_e32 v14, v5, v5
	v_mul_f32_e32 v15, v7, v7
	v_pk_add_f32 v[8:9], v[46:47], v[10:11]
	v_pk_add_f32 v[10:11], v[44:45], v[16:17]
	v_fmac_f32_e32 v14, v4, v4
	v_fmac_f32_e32 v15, v6, v6
	v_add_f32_e32 v14, v14, v15
	v_mul_f32_e32 v15, v11, v11
	v_mul_f32_e32 v16, v9, v9
	v_fmac_f32_e32 v15, v10, v10
	v_fmac_f32_e32 v16, v8, v8
	v_cvt_pk_bf16_f32 v4, v4, v5
	v_cvt_pk_bf16_f32 v5, v6, v7
	v_cvt_pk_bf16_f32 v6, v10, v11
	v_cvt_pk_bf16_f32 v7, v8, v9
	v_pk_add_f32 v[8:9], v[34:35], v[20:21]
	v_pk_add_f32 v[10:11], v[32:33], v[18:19]
	v_add_f32_e32 v15, v15, v16
	v_mul_f32_e32 v18, v11, v11
	v_mul_f32_e32 v19, v9, v9
	v_add_f32_e32 v26, v14, v15
	v_pk_add_f32 v[14:15], v[30:31], v[24:25]
	v_pk_add_f32 v[16:17], v[28:29], v[22:23]
	v_fmac_f32_e32 v18, v10, v10
	v_fmac_f32_e32 v19, v8, v8
	v_add_f32_e32 v18, v18, v19
	v_mul_f32_e32 v19, v17, v17
	v_mul_f32_e32 v20, v15, v15
	v_fmac_f32_e32 v19, v16, v16
	v_fmac_f32_e32 v20, v14, v14
	v_add_f32_e32 v19, v19, v20
	v_add_f32_e32 v18, v18, v19
	v_add_f32_e32 v18, v26, v18
	ds_bpermute_b32 v19, v190, v18
	s_waitcnt lgkmcnt(1)
	v_lshlrev_b64 v[12:13], 11, v[38:39]
	v_lshl_add_u64 v[12:13], v[12:13], 1, s[20:21]
	v_lshl_add_u64 v[12:13], v[36:37], 1, v[12:13]
	s_waitcnt lgkmcnt(0)
	global_store_dwordx4 v[208:209], v[246:249], off offset:256
	v_lshl_add_u64 v[208:209], v[12:13], 0, v[204:205]
	ds_bpermute_b32 v242, v203, v4
	ds_bpermute_b32 v243, v203, v5
	ds_bpermute_b32 v244, v203, v6
	ds_bpermute_b32 v245, v203, v7
	s_waitcnt lgkmcnt(0)
	s_nop 0
	v_add_f32_e32 v4, v18, v19
	ds_bpermute_b32 v5, v160, v4
	v_cvt_pk_bf16_f32 v6, v10, v11
	v_cvt_pk_bf16_f32 v7, v8, v9
	v_cvt_pk_bf16_f32 v8, v16, v17
	v_cvt_pk_bf16_f32 v9, v14, v15
	s_waitcnt lgkmcnt(0)
	global_store_dwordx4 v[208:209], v[242:245], off
	ds_bpermute_b32 v246, v203, v6
	ds_bpermute_b32 v247, v203, v7
	ds_bpermute_b32 v248, v203, v8
	ds_bpermute_b32 v249, v203, v9
	s_waitcnt lgkmcnt(0)
	global_store_dwordx4 v[208:209], v[246:249], off offset:256
	s_and_saveexec_b64 s[44:45], s[36:37]
	s_cbranch_execz .LBB0_838
	v_lshlrev_b64 v[6:7], 7, v[38:39]
	v_lshl_add_u64 v[6:7], s[22:23], 0, v[6:7]
	v_lshl_add_u64 v[6:7], s[42:43], 2, v[6:7]
	s_lshl_b32 s42, s62, 2
	s_mov_b32 s43, s31
	v_lshl_add_u64 v[6:7], v[6:7], 0, s[42:43]
	s_waitcnt lgkmcnt(0)
	v_add_f32_e32 v4, v4, v5
	global_store_dword v[6:7], v4, off
